# krope rewritten by hand: all 9 items per thread in flight (18 loads up front, counted waits), same arithmetic; on top of v5_ffta
# speedup vs baseline: 1.0077x; 1.0030x over previous
.LBB0_849:
	v_readlane_b32 s0, v254, 0
	v_readlane_b32 s1, v254, 1
	s_mov_b32 s2, s84
	v_mov_b32_e32 v2, v0
	s_nop 0
	v_lshl_add_u32 v8, s2, 9, v2
	s_mov_b32 s2, 0x108000
	v_cmp_gt_i32_e32 vcc, s2, v8
	s_and_saveexec_b64 s[2:3], vcc
	s_xor_b64 s[2:3], exec, s[2:3]
	s_cbranch_execz .LBB0_859
	s_load_dwordx2 s[12:13], s[0:1], 0xc8
	s_mov_b64 s[38:39], 0
	s_waitcnt lgkmcnt(0)
	s_add_u32 s14, s12, 0x3e31b000
	s_addc_u32 s15, s13, 0
	s_add_u32 s34, s12, 0xec000
	s_addc_u32 s35, s13, 0
	v_readlane_b32 s0, v254, 4
	v_readlane_b32 s1, v254, 5
	s_load_dword s0, s[0:1], 0x0
	s_waitcnt lgkmcnt(0)
	s_lshl_b32 s7, s0, 9
	v_mov_b32_e32 v20, v8
	v_add_u32_e32 v21, s7, v20
	v_add_u32_e32 v22, s7, v21
	v_add_u32_e32 v23, s7, v22
	v_add_u32_e32 v24, s7, v23
	v_add_u32_e32 v25, s7, v24
	v_add_u32_e32 v26, s7, v25
	v_add_u32_e32 v27, s7, v26
	v_add_u32_e32 v28, s7, v27
	s_mov_b32 s0, 0x1f41bf00
	s_mov_b32 s1, 0x3e0f83e1
	s_mov_b32 s7, 0x108000
	v_lshrrev_b32_e32 v4, 4, v20
	v_and_b32_e32 v5, 15, v20
	v_lshlrev_b32_e32 v6, 12, v4
	v_lshl_add_u32 v6, v5, 2, v6
	v_add_u32_e32 v30, s0, v6
	global_load_dword v40, v30, s[12:13]
	v_mul_hi_i32 v6, v4, s1
	v_cmp_gt_u32_e32 vcc, 8, v5
	v_ashrrev_i32_e32 v6, 11, v6
	v_mul_u32_u24_e32 v6, 0x2100, v6
	v_sub_u32_e32 v50, v4, v6
	v_add_u32_e32 v6, 0xffffff00, v50
	v_max_i32_e32 v6, 0, v6
	v_lshrrev_b32_e32 v7, 6, v6
	v_lshl_add_u32 v7, v7, 3, v5
	v_and_b32_e32 v6, 63, v6
	v_lshl_add_u32 v6, v6, 3, v5
	v_add_u32_e32 v6, 0x3f8, v6
	v_cndmask_b32_e32 v6, v6, v7, vcc
	v_lshlrev_b32_e32 v60, 3, v6
	global_load_dwordx2 v[70:71], v60, s[34:35]
	v_lshrrev_b32_e32 v4, 4, v21
	v_and_b32_e32 v5, 15, v21
	v_lshlrev_b32_e32 v6, 12, v4
	v_lshl_add_u32 v6, v5, 2, v6
	v_add_u32_e32 v31, s0, v6
	global_load_dword v41, v31, s[12:13]
	v_mul_hi_i32 v6, v4, s1
	v_cmp_gt_u32_e32 vcc, 8, v5
	v_ashrrev_i32_e32 v6, 11, v6
	v_mul_u32_u24_e32 v6, 0x2100, v6
	v_sub_u32_e32 v51, v4, v6
	v_add_u32_e32 v6, 0xffffff00, v51
	v_max_i32_e32 v6, 0, v6
	v_lshrrev_b32_e32 v7, 6, v6
	v_lshl_add_u32 v7, v7, 3, v5
	v_and_b32_e32 v6, 63, v6
	v_lshl_add_u32 v6, v6, 3, v5
	v_add_u32_e32 v6, 0x3f8, v6
	v_cndmask_b32_e32 v6, v6, v7, vcc
	v_lshlrev_b32_e32 v61, 3, v6
	global_load_dwordx2 v[72:73], v61, s[34:35]
	v_lshrrev_b32_e32 v4, 4, v22
	v_and_b32_e32 v5, 15, v22
	v_lshlrev_b32_e32 v6, 12, v4
	v_lshl_add_u32 v6, v5, 2, v6
	v_add_u32_e32 v32, s0, v6
	global_load_dword v42, v32, s[12:13]
	v_mul_hi_i32 v6, v4, s1
	v_cmp_gt_u32_e32 vcc, 8, v5
	v_ashrrev_i32_e32 v6, 11, v6
	v_mul_u32_u24_e32 v6, 0x2100, v6
	v_sub_u32_e32 v52, v4, v6
	v_add_u32_e32 v6, 0xffffff00, v52
	v_max_i32_e32 v6, 0, v6
	v_lshrrev_b32_e32 v7, 6, v6
	v_lshl_add_u32 v7, v7, 3, v5
	v_and_b32_e32 v6, 63, v6
	v_lshl_add_u32 v6, v6, 3, v5
	v_add_u32_e32 v6, 0x3f8, v6
	v_cndmask_b32_e32 v6, v6, v7, vcc
	v_lshlrev_b32_e32 v62, 3, v6
	global_load_dwordx2 v[74:75], v62, s[34:35]
	v_lshrrev_b32_e32 v4, 4, v23
	v_and_b32_e32 v5, 15, v23
	v_lshlrev_b32_e32 v6, 12, v4
	v_lshl_add_u32 v6, v5, 2, v6
	v_add_u32_e32 v33, s0, v6
	global_load_dword v43, v33, s[12:13]
	v_mul_hi_i32 v6, v4, s1
	v_cmp_gt_u32_e32 vcc, 8, v5
	v_ashrrev_i32_e32 v6, 11, v6
	v_mul_u32_u24_e32 v6, 0x2100, v6
	v_sub_u32_e32 v53, v4, v6
	v_add_u32_e32 v6, 0xffffff00, v53
	v_max_i32_e32 v6, 0, v6
	v_lshrrev_b32_e32 v7, 6, v6
	v_lshl_add_u32 v7, v7, 3, v5
	v_and_b32_e32 v6, 63, v6
	v_lshl_add_u32 v6, v6, 3, v5
	v_add_u32_e32 v6, 0x3f8, v6
	v_cndmask_b32_e32 v6, v6, v7, vcc
	v_lshlrev_b32_e32 v63, 3, v6
	global_load_dwordx2 v[76:77], v63, s[34:35]
	v_lshrrev_b32_e32 v4, 4, v24
	v_and_b32_e32 v5, 15, v24
	v_lshlrev_b32_e32 v6, 12, v4
	v_lshl_add_u32 v6, v5, 2, v6
	v_add_u32_e32 v34, s0, v6
	global_load_dword v44, v34, s[12:13]
	v_mul_hi_i32 v6, v4, s1
	v_cmp_gt_u32_e32 vcc, 8, v5
	v_ashrrev_i32_e32 v6, 11, v6
	v_mul_u32_u24_e32 v6, 0x2100, v6
	v_sub_u32_e32 v54, v4, v6
	v_add_u32_e32 v6, 0xffffff00, v54
	v_max_i32_e32 v6, 0, v6
	v_lshrrev_b32_e32 v7, 6, v6
	v_lshl_add_u32 v7, v7, 3, v5
	v_and_b32_e32 v6, 63, v6
	v_lshl_add_u32 v6, v6, 3, v5
	v_add_u32_e32 v6, 0x3f8, v6
	v_cndmask_b32_e32 v6, v6, v7, vcc
	v_lshlrev_b32_e32 v64, 3, v6
	global_load_dwordx2 v[78:79], v64, s[34:35]
	v_lshrrev_b32_e32 v4, 4, v25
	v_and_b32_e32 v5, 15, v25
	v_lshlrev_b32_e32 v6, 12, v4
	v_lshl_add_u32 v6, v5, 2, v6
	v_add_u32_e32 v35, s0, v6
	global_load_dword v45, v35, s[12:13]
	v_mul_hi_i32 v6, v4, s1
	v_cmp_gt_u32_e32 vcc, 8, v5
	v_ashrrev_i32_e32 v6, 11, v6
	v_mul_u32_u24_e32 v6, 0x2100, v6
	v_sub_u32_e32 v55, v4, v6
	v_add_u32_e32 v6, 0xffffff00, v55
	v_max_i32_e32 v6, 0, v6
	v_lshrrev_b32_e32 v7, 6, v6
	v_lshl_add_u32 v7, v7, 3, v5
	v_and_b32_e32 v6, 63, v6
	v_lshl_add_u32 v6, v6, 3, v5
	v_add_u32_e32 v6, 0x3f8, v6
	v_cndmask_b32_e32 v6, v6, v7, vcc
	v_lshlrev_b32_e32 v65, 3, v6
	global_load_dwordx2 v[80:81], v65, s[34:35]
	v_lshrrev_b32_e32 v4, 4, v26
	v_and_b32_e32 v5, 15, v26
	v_lshlrev_b32_e32 v6, 12, v4
	v_lshl_add_u32 v6, v5, 2, v6
	v_add_u32_e32 v36, s0, v6
	global_load_dword v46, v36, s[12:13]
	v_mul_hi_i32 v6, v4, s1
	v_cmp_gt_u32_e32 vcc, 8, v5
	v_ashrrev_i32_e32 v6, 11, v6
	v_mul_u32_u24_e32 v6, 0x2100, v6
	v_sub_u32_e32 v56, v4, v6
	v_add_u32_e32 v6, 0xffffff00, v56
	v_max_i32_e32 v6, 0, v6
	v_lshrrev_b32_e32 v7, 6, v6
	v_lshl_add_u32 v7, v7, 3, v5
	v_and_b32_e32 v6, 63, v6
	v_lshl_add_u32 v6, v6, 3, v5
	v_add_u32_e32 v6, 0x3f8, v6
	v_cndmask_b32_e32 v6, v6, v7, vcc
	v_lshlrev_b32_e32 v66, 3, v6
	global_load_dwordx2 v[82:83], v66, s[34:35]
	v_lshrrev_b32_e32 v4, 4, v27
	v_and_b32_e32 v5, 15, v27
	v_lshlrev_b32_e32 v6, 12, v4
	v_lshl_add_u32 v6, v5, 2, v6
	v_add_u32_e32 v37, s0, v6
	global_load_dword v47, v37, s[12:13]
	v_mul_hi_i32 v6, v4, s1
	v_cmp_gt_u32_e32 vcc, 8, v5
	v_ashrrev_i32_e32 v6, 11, v6
	v_mul_u32_u24_e32 v6, 0x2100, v6
	v_sub_u32_e32 v57, v4, v6
	v_add_u32_e32 v6, 0xffffff00, v57
	v_max_i32_e32 v6, 0, v6
	v_lshrrev_b32_e32 v7, 6, v6
	v_lshl_add_u32 v7, v7, 3, v5
	v_and_b32_e32 v6, 63, v6
	v_lshl_add_u32 v6, v6, 3, v5
	v_add_u32_e32 v6, 0x3f8, v6
	v_cndmask_b32_e32 v6, v6, v7, vcc
	v_lshlrev_b32_e32 v67, 3, v6
	global_load_dwordx2 v[84:85], v67, s[34:35]
	v_lshrrev_b32_e32 v4, 4, v28
	v_and_b32_e32 v5, 15, v28
	v_lshlrev_b32_e32 v6, 12, v4
	v_lshl_add_u32 v6, v5, 2, v6
	v_add_u32_e32 v38, s0, v6
	v_cmp_gt_i32_e32 vcc, s7, v28
	s_nop 1
	s_and_saveexec_b64 s[20:21], vcc
	global_load_dword v48, v38, s[12:13]
	v_mul_hi_i32 v6, v4, s1
	v_cmp_gt_u32_e32 vcc, 8, v5
	v_ashrrev_i32_e32 v6, 11, v6
	v_mul_u32_u24_e32 v6, 0x2100, v6
	v_sub_u32_e32 v58, v4, v6
	v_add_u32_e32 v6, 0xffffff00, v58
	v_max_i32_e32 v6, 0, v6
	v_lshrrev_b32_e32 v7, 6, v6
	v_lshl_add_u32 v7, v7, 3, v5
	v_and_b32_e32 v6, 63, v6
	v_lshl_add_u32 v6, v6, 3, v5
	v_add_u32_e32 v6, 0x3f8, v6
	v_cndmask_b32_e32 v6, v6, v7, vcc
	v_lshlrev_b32_e32 v68, 3, v6
	global_load_dwordx2 v[86:87], v68, s[34:35]
	s_or_b64 exec, exec, s[20:21]
	s_mov_b32 s0, 0x3e31b000
	s_waitcnt vmcnt(16)
	v_lshlrev_b32_e32 v4, 16, v40
	v_and_b32_e32 v5, 0xffff0000, v40
	v_cmp_lt_u32_e32 vcc, 0xff, v50
	v_mul_f32_e32 v6, v70, v4
	v_mul_f32_e32 v7, v71, v5
	v_sub_f32_e32 v6, v6, v7
	v_mul_f32_e32 v7, v70, v5
	v_fma_f32 v7, v71, v4, v7
	v_cndmask_b32_e32 v6, v4, v6, vcc
	v_cndmask_b32_e32 v7, v5, v7, vcc
	v_lshlrev_b32_e32 v4, 2, v20
	v_cvt_pk_bf16_f32 v6, v6, v7
	v_add_u32_e32 v4, s0, v4
	global_store_dword v4, v6, s[12:13]
	s_waitcnt vmcnt(14)
	v_lshlrev_b32_e32 v4, 16, v41
	v_and_b32_e32 v5, 0xffff0000, v41
	v_cmp_lt_u32_e32 vcc, 0xff, v51
	v_mul_f32_e32 v6, v72, v4
	v_mul_f32_e32 v7, v73, v5
	v_sub_f32_e32 v6, v6, v7
	v_mul_f32_e32 v7, v72, v5
	v_fma_f32 v7, v73, v4, v7
	v_cndmask_b32_e32 v6, v4, v6, vcc
	v_cndmask_b32_e32 v7, v5, v7, vcc
	v_lshlrev_b32_e32 v4, 2, v21
	v_cvt_pk_bf16_f32 v6, v6, v7
	v_add_u32_e32 v4, s0, v4
	global_store_dword v4, v6, s[12:13]
	s_waitcnt vmcnt(12)
	v_lshlrev_b32_e32 v4, 16, v42
	v_and_b32_e32 v5, 0xffff0000, v42
	v_cmp_lt_u32_e32 vcc, 0xff, v52
	v_mul_f32_e32 v6, v74, v4
	v_mul_f32_e32 v7, v75, v5
	v_sub_f32_e32 v6, v6, v7
	v_mul_f32_e32 v7, v74, v5
	v_fma_f32 v7, v75, v4, v7
	v_cndmask_b32_e32 v6, v4, v6, vcc
	v_cndmask_b32_e32 v7, v5, v7, vcc
	v_lshlrev_b32_e32 v4, 2, v22
	v_cvt_pk_bf16_f32 v6, v6, v7
	v_add_u32_e32 v4, s0, v4
	global_store_dword v4, v6, s[12:13]
	s_waitcnt vmcnt(10)
	v_lshlrev_b32_e32 v4, 16, v43
	v_and_b32_e32 v5, 0xffff0000, v43
	v_cmp_lt_u32_e32 vcc, 0xff, v53
	v_mul_f32_e32 v6, v76, v4
	v_mul_f32_e32 v7, v77, v5
	v_sub_f32_e32 v6, v6, v7
	v_mul_f32_e32 v7, v76, v5
	v_fma_f32 v7, v77, v4, v7
	v_cndmask_b32_e32 v6, v4, v6, vcc
	v_cndmask_b32_e32 v7, v5, v7, vcc
	v_lshlrev_b32_e32 v4, 2, v23
	v_cvt_pk_bf16_f32 v6, v6, v7
	v_add_u32_e32 v4, s0, v4
	global_store_dword v4, v6, s[12:13]
	s_waitcnt vmcnt(8)
	v_lshlrev_b32_e32 v4, 16, v44
	v_and_b32_e32 v5, 0xffff0000, v44
	v_cmp_lt_u32_e32 vcc, 0xff, v54
	v_mul_f32_e32 v6, v78, v4
	v_mul_f32_e32 v7, v79, v5
	v_sub_f32_e32 v6, v6, v7
	v_mul_f32_e32 v7, v78, v5
	v_fma_f32 v7, v79, v4, v7
	v_cndmask_b32_e32 v6, v4, v6, vcc
	v_cndmask_b32_e32 v7, v5, v7, vcc
	v_lshlrev_b32_e32 v4, 2, v24
	v_cvt_pk_bf16_f32 v6, v6, v7
	v_add_u32_e32 v4, s0, v4
	global_store_dword v4, v6, s[12:13]
	s_waitcnt vmcnt(6)
	v_lshlrev_b32_e32 v4, 16, v45
	v_and_b32_e32 v5, 0xffff0000, v45
	v_cmp_lt_u32_e32 vcc, 0xff, v55
	v_mul_f32_e32 v6, v80, v4
	v_mul_f32_e32 v7, v81, v5
	v_sub_f32_e32 v6, v6, v7
	v_mul_f32_e32 v7, v80, v5
	v_fma_f32 v7, v81, v4, v7
	v_cndmask_b32_e32 v6, v4, v6, vcc
	v_cndmask_b32_e32 v7, v5, v7, vcc
	v_lshlrev_b32_e32 v4, 2, v25
	v_cvt_pk_bf16_f32 v6, v6, v7
	v_add_u32_e32 v4, s0, v4
	global_store_dword v4, v6, s[12:13]
	s_waitcnt vmcnt(4)
	v_lshlrev_b32_e32 v4, 16, v46
	v_and_b32_e32 v5, 0xffff0000, v46
	v_cmp_lt_u32_e32 vcc, 0xff, v56
	v_mul_f32_e32 v6, v82, v4
	v_mul_f32_e32 v7, v83, v5
	v_sub_f32_e32 v6, v6, v7
	v_mul_f32_e32 v7, v82, v5
	v_fma_f32 v7, v83, v4, v7
	v_cndmask_b32_e32 v6, v4, v6, vcc
	v_cndmask_b32_e32 v7, v5, v7, vcc
	v_lshlrev_b32_e32 v4, 2, v26
	v_cvt_pk_bf16_f32 v6, v6, v7
	v_add_u32_e32 v4, s0, v4
	global_store_dword v4, v6, s[12:13]
	s_waitcnt vmcnt(2)
	v_lshlrev_b32_e32 v4, 16, v47
	v_and_b32_e32 v5, 0xffff0000, v47
	v_cmp_lt_u32_e32 vcc, 0xff, v57
	v_mul_f32_e32 v6, v84, v4
	v_mul_f32_e32 v7, v85, v5
	v_sub_f32_e32 v6, v6, v7
	v_mul_f32_e32 v7, v84, v5
	v_fma_f32 v7, v85, v4, v7
	v_cndmask_b32_e32 v6, v4, v6, vcc
	v_cndmask_b32_e32 v7, v5, v7, vcc
	v_lshlrev_b32_e32 v4, 2, v27
	v_cvt_pk_bf16_f32 v6, v6, v7
	v_add_u32_e32 v4, s0, v4
	global_store_dword v4, v6, s[12:13]
	v_cmp_gt_i32_e32 vcc, s7, v28
	s_nop 1
	s_and_saveexec_b64 s[20:21], vcc
	s_waitcnt vmcnt(0)
	v_lshlrev_b32_e32 v4, 16, v48
	v_and_b32_e32 v5, 0xffff0000, v48
	v_cmp_lt_u32_e32 vcc, 0xff, v58
	v_mul_f32_e32 v6, v86, v4
	v_mul_f32_e32 v7, v87, v5
	v_sub_f32_e32 v6, v6, v7
	v_mul_f32_e32 v7, v86, v5
	v_fma_f32 v7, v87, v4, v7
	v_cndmask_b32_e32 v6, v4, v6, vcc
	v_cndmask_b32_e32 v7, v5, v7, vcc
	v_lshlrev_b32_e32 v4, 2, v28
	v_cvt_pk_bf16_f32 v6, v6, v7
	v_add_u32_e32 v4, s0, v4
	global_store_dword v4, v6, s[12:13]
	s_or_b64 exec, exec, s[20:21]
